# speedup vs baseline: 1.0220x; 1.0010x over previous
.LBB2_4:
	ds_read_b128 v[114:117], v108 offset:16384
	ds_read_b128 v[118:121], v108 offset:17408
	ds_read_b128 v[122:125], v108 offset:18432
	ds_read_b128 v[126:129], v108 offset:19456
	s_add_i32 s43, s29, -1
	s_min_i32 s16, s43, s34
	s_min_i32 s14, s29, s34
	s_ashr_i32 s17, s16, 31
	s_ashr_i32 s15, s14, 31
	s_lshl_b64 s[16:17], s[16:17], 11
	s_mov_b32 m0, s35
	v_lshl_add_u64 v[166:167], s[6:7], 0, v[100:101]
	ds_read_b128 v[134:137], v109
	ds_read_b128 v[138:141], v109 offset:1024
	ds_read_b128 v[142:145], v109 offset:2048
	ds_read_b128 v[146:149], v109 offset:3072
	ds_read_b128 v[150:153], v109 offset:4096
	ds_read_b128 v[154:157], v109 offset:5120
	ds_read_b128 v[158:161], v109 offset:6144
	ds_read_b128 v[162:165], v109 offset:7168
	global_load_lds_dwordx4 v[166:167], off
	v_lshl_add_u64 v[166:167], s[6:7], 0, v[102:103]
	s_mov_b32 m0, s36
	s_nop 0
	global_load_lds_dwordx4 v[166:167], off
	s_waitcnt vmcnt(8)
	s_barrier
	s_waitcnt lgkmcnt(0)
	s_waitcnt lgkmcnt(0)
	v_mfma_f32_16x16x32_f16 v[94:97], v[114:117], v[134:137], v[94:97]
	v_mfma_f32_16x16x32_f16 v[90:93], v[122:125], v[134:137], v[90:93]
	v_mfma_f32_16x16x32_f16 v[86:89], v[114:117], v[142:145], v[86:89]
	v_mfma_f32_16x16x32_f16 v[82:85], v[122:125], v[142:145], v[82:85]
	v_mfma_f32_16x16x32_f16 v[78:81], v[114:117], v[150:153], v[78:81]
	v_mfma_f32_16x16x32_f16 v[74:77], v[122:125], v[150:153], v[74:77]
	v_mfma_f32_16x16x32_f16 v[70:73], v[114:117], v[158:161], v[70:73]
	v_mfma_f32_16x16x32_f16 v[66:69], v[122:125], v[158:161], v[66:69]
	v_mfma_f32_16x16x32_f16 v[94:97], v[118:121], v[138:141], v[94:97]
	v_mfma_f32_16x16x32_f16 v[90:93], v[126:129], v[138:141], v[90:93]
	v_mfma_f32_16x16x32_f16 v[86:89], v[118:121], v[146:149], v[86:89]
	v_mfma_f32_16x16x32_f16 v[82:85], v[126:129], v[146:149], v[82:85]
	v_mfma_f32_16x16x32_f16 v[78:81], v[118:121], v[154:157], v[78:81]
	v_mfma_f32_16x16x32_f16 v[74:77], v[126:129], v[154:157], v[74:77]
	v_mfma_f32_16x16x32_f16 v[70:73], v[118:121], v[162:165], v[70:73]
	v_mfma_f32_16x16x32_f16 v[66:69], v[126:129], v[162:165], v[66:69]
	s_barrier
	s_mov_b32 m0, s37
	v_lshl_add_u64 v[166:167], s[6:7], 0, v[104:105]
	ds_read_b128 v[114:117], v108 offset:32768
	ds_read_b128 v[118:121], v108 offset:33792
	ds_read_b128 v[122:125], v108 offset:34816
	ds_read_b128 v[126:129], v108 offset:35840
	global_load_lds_dwordx4 v[166:167], off
	v_lshl_add_u64 v[166:167], s[6:7], 0, v[106:107]
	s_mov_b32 m0, s38
	s_nop 0
	global_load_lds_dwordx4 v[166:167], off
	s_waitcnt vmcnt(8)
	s_barrier
	s_waitcnt lgkmcnt(0)
	s_waitcnt lgkmcnt(0)
	v_mfma_f32_16x16x32_f16 v[62:65], v[114:117], v[134:137], v[62:65]
	v_mfma_f32_16x16x32_f16 v[58:61], v[122:125], v[134:137], v[58:61]
	v_mfma_f32_16x16x32_f16 v[54:57], v[114:117], v[142:145], v[54:57]
	v_mfma_f32_16x16x32_f16 v[50:53], v[122:125], v[142:145], v[50:53]
	v_mfma_f32_16x16x32_f16 v[46:49], v[114:117], v[150:153], v[46:49]
	v_mfma_f32_16x16x32_f16 v[42:45], v[122:125], v[150:153], v[42:45]
	v_mfma_f32_16x16x32_f16 v[38:41], v[114:117], v[158:161], v[38:41]
	v_mfma_f32_16x16x32_f16 v[34:37], v[122:125], v[158:161], v[34:37]
	v_mfma_f32_16x16x32_f16 v[62:65], v[118:121], v[138:141], v[62:65]
	v_mfma_f32_16x16x32_f16 v[58:61], v[126:129], v[138:141], v[58:61]
	v_mfma_f32_16x16x32_f16 v[54:57], v[118:121], v[146:149], v[54:57]
	v_mfma_f32_16x16x32_f16 v[50:53], v[126:129], v[146:149], v[50:53]
	v_mfma_f32_16x16x32_f16 v[46:49], v[118:121], v[154:157], v[46:49]
	v_mfma_f32_16x16x32_f16 v[42:45], v[126:129], v[154:157], v[42:45]
	v_mfma_f32_16x16x32_f16 v[38:41], v[118:121], v[162:165], v[38:41]
	v_mfma_f32_16x16x32_f16 v[34:37], v[126:129], v[162:165], v[34:37]
	s_barrier
	s_add_u32 s44, s4, s16
	s_addc_u32 s45, s5, s17
	s_mov_b32 m0, s18
	v_lshl_add_u64 v[166:167], s[44:45], 0, v[130:131]
	ds_read_b128 v[114:117], v108 offset:49152
	ds_read_b128 v[118:121], v108 offset:50176
	ds_read_b128 v[122:125], v108 offset:51200
	ds_read_b128 v[126:129], v108 offset:52224
	global_load_lds_dwordx4 v[166:167], off
	v_lshl_add_u64 v[166:167], s[44:45], 0, v[98:99]
	s_add_u32 s44, s8, s16
	s_mov_b32 m0, s19
	s_addc_u32 s45, s9, s17
	global_load_lds_dwordx4 v[166:167], off
	v_lshl_add_u64 v[166:167], s[44:45], 0, v[130:131]
	s_mov_b32 m0, s20
	s_nop 0
	global_load_lds_dwordx4 v[166:167], off
	v_lshl_add_u64 v[166:167], s[44:45], 0, v[98:99]
	s_mov_b32 m0, s21
	s_nop 0
	global_load_lds_dwordx4 v[166:167], off
	s_waitcnt vmcnt(8)
	s_barrier
	s_waitcnt lgkmcnt(0)
	s_waitcnt lgkmcnt(0)
	v_mfma_f32_16x16x32_f16 v[30:33], v[114:117], v[134:137], v[30:33]
	v_mfma_f32_16x16x32_f16 v[26:29], v[122:125], v[134:137], v[26:29]
	v_mfma_f32_16x16x32_f16 v[22:25], v[114:117], v[142:145], v[22:25]
	v_mfma_f32_16x16x32_f16 v[18:21], v[122:125], v[142:145], v[18:21]
	v_mfma_f32_16x16x32_f16 v[14:17], v[114:117], v[150:153], v[14:17]
	v_mfma_f32_16x16x32_f16 v[10:13], v[122:125], v[150:153], v[10:13]
	v_mfma_f32_16x16x32_f16 v[6:9], v[114:117], v[158:161], v[6:9]
	v_mfma_f32_16x16x32_f16 v[2:5], v[122:125], v[158:161], v[2:5]
	v_mfma_f32_16x16x32_f16 v[30:33], v[118:121], v[138:141], v[30:33]
	v_mfma_f32_16x16x32_f16 v[26:29], v[126:129], v[138:141], v[26:29]
	v_mfma_f32_16x16x32_f16 v[22:25], v[118:121], v[146:149], v[22:25]
	v_mfma_f32_16x16x32_f16 v[18:21], v[126:129], v[146:149], v[18:21]
	v_mfma_f32_16x16x32_f16 v[14:17], v[118:121], v[154:157], v[14:17]
	v_mfma_f32_16x16x32_f16 v[10:13], v[126:129], v[154:157], v[10:13]
	v_mfma_f32_16x16x32_f16 v[6:9], v[118:121], v[162:165], v[6:9]
	v_mfma_f32_16x16x32_f16 v[2:5], v[126:129], v[162:165], v[2:5]
	s_barrier
	ds_read_b128 v[114:117], v110
	ds_read_b128 v[118:121], v110 offset:1024
	ds_read_b128 v[122:125], v110 offset:2048
	ds_read_b128 v[126:129], v110 offset:3072
	s_add_u32 s44, s10, s16
	s_addc_u32 s45, s11, s17
	s_mov_b32 m0, s22
	v_lshl_add_u64 v[166:167], s[44:45], 0, v[130:131]
	ds_read_b128 v[134:137], v111
	ds_read_b128 v[138:141], v111 offset:1024
	ds_read_b128 v[142:145], v111 offset:2048
	ds_read_b128 v[146:149], v111 offset:3072
	ds_read_b128 v[150:153], v111 offset:4096
	ds_read_b128 v[154:157], v111 offset:5120
	ds_read_b128 v[158:161], v111 offset:6144
	ds_read_b128 v[162:165], v111 offset:7168
	global_load_lds_dwordx4 v[166:167], off
	v_lshl_add_u64 v[166:167], s[44:45], 0, v[98:99]
	s_mov_b32 m0, s23
	s_nop 0
	global_load_lds_dwordx4 v[166:167], off
	s_waitcnt vmcnt(8)
	s_barrier
	s_waitcnt lgkmcnt(0)
	s_waitcnt lgkmcnt(0)
	v_mfma_f32_16x16x32_f16 v[94:97], v[114:117], v[134:137], v[94:97]
	v_mfma_f32_16x16x32_f16 v[90:93], v[122:125], v[134:137], v[90:93]
	v_mfma_f32_16x16x32_f16 v[86:89], v[114:117], v[142:145], v[86:89]
	v_mfma_f32_16x16x32_f16 v[82:85], v[122:125], v[142:145], v[82:85]
	v_mfma_f32_16x16x32_f16 v[78:81], v[114:117], v[150:153], v[78:81]
	v_mfma_f32_16x16x32_f16 v[74:77], v[122:125], v[150:153], v[74:77]
	v_mfma_f32_16x16x32_f16 v[70:73], v[114:117], v[158:161], v[70:73]
	v_mfma_f32_16x16x32_f16 v[66:69], v[122:125], v[158:161], v[66:69]
	v_mfma_f32_16x16x32_f16 v[94:97], v[118:121], v[138:141], v[94:97]
	v_mfma_f32_16x16x32_f16 v[90:93], v[126:129], v[138:141], v[90:93]
	v_mfma_f32_16x16x32_f16 v[86:89], v[118:121], v[146:149], v[86:89]
	v_mfma_f32_16x16x32_f16 v[82:85], v[126:129], v[146:149], v[82:85]
	v_mfma_f32_16x16x32_f16 v[78:81], v[118:121], v[154:157], v[78:81]
	v_mfma_f32_16x16x32_f16 v[74:77], v[126:129], v[154:157], v[74:77]
	v_mfma_f32_16x16x32_f16 v[70:73], v[118:121], v[162:165], v[70:73]
	v_mfma_f32_16x16x32_f16 v[66:69], v[126:129], v[162:165], v[66:69]
	s_barrier
	s_add_u32 s16, s12, s16
	s_addc_u32 s17, s13, s17
	s_mov_b32 m0, s26
	v_lshl_add_u64 v[166:167], s[16:17], 0, v[130:131]
	ds_read_b128 v[114:117], v112
	ds_read_b128 v[118:121], v112 offset:1024
	ds_read_b128 v[122:125], v112 offset:2048
	ds_read_b128 v[126:129], v112 offset:3072
	global_load_lds_dwordx4 v[166:167], off
	v_lshl_add_u64 v[166:167], s[16:17], 0, v[98:99]
	s_mov_b32 m0, s27
	s_nop 0
	global_load_lds_dwordx4 v[166:167], off
	s_waitcnt vmcnt(8)
	s_barrier
	s_waitcnt lgkmcnt(0)
	s_waitcnt lgkmcnt(0)
	v_mfma_f32_16x16x32_f16 v[62:65], v[114:117], v[134:137], v[62:65]
	v_mfma_f32_16x16x32_f16 v[58:61], v[122:125], v[134:137], v[58:61]
	v_mfma_f32_16x16x32_f16 v[54:57], v[114:117], v[142:145], v[54:57]
	v_mfma_f32_16x16x32_f16 v[50:53], v[122:125], v[142:145], v[50:53]
	v_mfma_f32_16x16x32_f16 v[46:49], v[114:117], v[150:153], v[46:49]
	v_mfma_f32_16x16x32_f16 v[42:45], v[122:125], v[150:153], v[42:45]
	v_mfma_f32_16x16x32_f16 v[38:41], v[114:117], v[158:161], v[38:41]
	v_mfma_f32_16x16x32_f16 v[34:37], v[122:125], v[158:161], v[34:37]
	v_mfma_f32_16x16x32_f16 v[62:65], v[118:121], v[138:141], v[62:65]
	v_mfma_f32_16x16x32_f16 v[58:61], v[126:129], v[138:141], v[58:61]
	v_mfma_f32_16x16x32_f16 v[54:57], v[118:121], v[146:149], v[54:57]
	v_mfma_f32_16x16x32_f16 v[50:53], v[126:129], v[146:149], v[50:53]
	v_mfma_f32_16x16x32_f16 v[46:49], v[118:121], v[154:157], v[46:49]
	v_mfma_f32_16x16x32_f16 v[42:45], v[126:129], v[154:157], v[42:45]
	v_mfma_f32_16x16x32_f16 v[38:41], v[118:121], v[162:165], v[38:41]
	v_mfma_f32_16x16x32_f16 v[34:37], v[126:129], v[162:165], v[34:37]
	s_barrier
	s_lshl_b64 s[14:15], s[14:15], 11
	s_add_u32 s16, s4, s14
	s_addc_u32 s17, s5, s15
	s_mov_b32 m0, s39
	v_lshl_add_u64 v[166:167], s[16:17], 0, v[130:131]
	s_add_u32 s14, s8, s14
	ds_read_b128 v[114:117], v113
	ds_read_b128 v[118:121], v113 offset:1024
	ds_read_b128 v[122:125], v113 offset:2048
	ds_read_b128 v[126:129], v113 offset:3072
	global_load_lds_dwordx4 v[166:167], off
	v_lshl_add_u64 v[166:167], s[16:17], 0, v[98:99]
	s_mov_b32 m0, s40
	s_addc_u32 s15, s9, s15
	global_load_lds_dwordx4 v[166:167], off
	v_lshl_add_u64 v[166:167], s[14:15], 0, v[130:131]
	s_mov_b32 m0, s41
	s_nop 0
	global_load_lds_dwordx4 v[166:167], off
	v_lshl_add_u64 v[166:167], s[14:15], 0, v[98:99]
	s_mov_b32 m0, s42
	s_nop 0
	global_load_lds_dwordx4 v[166:167], off
	s_waitcnt vmcnt(8)
	s_barrier
	s_waitcnt lgkmcnt(0)
	s_waitcnt lgkmcnt(0)
	v_mfma_f32_16x16x32_f16 v[30:33], v[114:117], v[134:137], v[30:33]
	v_mfma_f32_16x16x32_f16 v[26:29], v[122:125], v[134:137], v[26:29]
	v_mfma_f32_16x16x32_f16 v[22:25], v[114:117], v[142:145], v[22:25]
	v_mfma_f32_16x16x32_f16 v[18:21], v[122:125], v[142:145], v[18:21]
	v_mfma_f32_16x16x32_f16 v[14:17], v[114:117], v[150:153], v[14:17]
	v_mfma_f32_16x16x32_f16 v[10:13], v[122:125], v[150:153], v[10:13]
	v_mfma_f32_16x16x32_f16 v[6:9], v[114:117], v[158:161], v[6:9]
	v_mfma_f32_16x16x32_f16 v[2:5], v[122:125], v[158:161], v[2:5]
	v_mfma_f32_16x16x32_f16 v[30:33], v[118:121], v[138:141], v[30:33]
	v_mfma_f32_16x16x32_f16 v[26:29], v[126:129], v[138:141], v[26:29]
	v_mfma_f32_16x16x32_f16 v[22:25], v[118:121], v[146:149], v[22:25]
	v_mfma_f32_16x16x32_f16 v[18:21], v[126:129], v[146:149], v[18:21]
	v_mfma_f32_16x16x32_f16 v[14:17], v[118:121], v[154:157], v[14:17]
	v_mfma_f32_16x16x32_f16 v[10:13], v[126:129], v[154:157], v[10:13]
	v_mfma_f32_16x16x32_f16 v[6:9], v[118:121], v[162:165], v[6:9]
	v_mfma_f32_16x16x32_f16 v[2:5], v[126:129], v[162:165], v[2:5]
	s_barrier
	s_add_u32 s6, s6, 0x1000
	s_addc_u32 s7, s7, 0
	s_add_i32 s29, s29, 2
	s_cmp_ge_i32 s43, s33
	s_cbranch_scc0 .LBB2_4
	v_mov_b32_e32 v131, v97

.LBB3_4:
	v_add_u32_e32 v73, s16, v72
	ds_read_b128 v[74:77], v73 offset:16384
	ds_read_b128 v[78:81], v73 offset:17408
	ds_read_b128 v[82:85], v73 offset:18432
	ds_read_b128 v[86:89], v73 offset:19456
	s_add_i32 s18, s15, 2
	s_min_i32 s18, s18, s9
	s_ashr_i32 s19, s18, 31
	s_lshl_b64 s[18:19], s[18:19], 11
	s_add_u32 s20, s4, s18
	s_addc_u32 s21, s5, s19
	s_add_i32 s17, s14, s17
	v_add_u32_e32 v118, s16, v67
	v_lshl_add_u64 v[122:123], s[20:21], 0, v[68:69]
	s_mov_b32 m0, s17
	ds_read_b128 v[90:93], v118
	ds_read_b128 v[94:97], v118 offset:1024
	ds_read_b128 v[98:101], v118 offset:2048
	ds_read_b128 v[102:105], v118 offset:3072
	ds_read_b128 v[106:109], v118 offset:4096
	ds_read_b128 v[110:113], v118 offset:5120
	ds_read_b128 v[114:117], v118 offset:6144
	ds_read_b128 v[118:121], v118 offset:7168
	global_load_lds_dwordx4 v[122:123], off
	s_add_i32 m0, s17, 0x2000
	s_add_u32 s18, s6, s18
	v_lshl_add_u64 v[122:123], s[20:21], 0, v[70:71]
	s_addc_u32 s19, s7, s19
	global_load_lds_dwordx4 v[122:123], off
	s_add_i32 m0, s17, 0x4000
	v_lshl_add_u64 v[122:123], s[18:19], 0, v[68:69]
	global_load_lds_dwordx4 v[122:123], off
	v_lshl_add_u64 v[122:123], s[18:19], 0, v[70:71]
	s_add_i32 m0, s17, 0x6000
	s_nop 0
	global_load_lds_dwordx4 v[122:123], off
	s_waitcnt vmcnt(10)
	s_barrier
	s_waitcnt lgkmcnt(0)
	s_waitcnt lgkmcnt(0)
	v_mfma_f32_16x16x32_f16 v[62:65], v[74:77], v[90:93], v[62:65]
	v_mfma_f32_16x16x32_f16 v[46:49], v[82:85], v[90:93], v[46:49]
	v_mfma_f32_16x16x32_f16 v[58:61], v[74:77], v[98:101], v[58:61]
	v_mfma_f32_16x16x32_f16 v[42:45], v[82:85], v[98:101], v[42:45]
	v_mfma_f32_16x16x32_f16 v[54:57], v[74:77], v[106:109], v[54:57]
	v_mfma_f32_16x16x32_f16 v[38:41], v[82:85], v[106:109], v[38:41]
	v_mfma_f32_16x16x32_f16 v[50:53], v[74:77], v[114:117], v[50:53]
	v_mfma_f32_16x16x32_f16 v[26:29], v[82:85], v[114:117], v[26:29]
	v_mfma_f32_16x16x32_f16 v[62:65], v[78:81], v[94:97], v[62:65]
	v_mfma_f32_16x16x32_f16 v[46:49], v[86:89], v[94:97], v[46:49]
	v_mfma_f32_16x16x32_f16 v[58:61], v[78:81], v[102:105], v[58:61]
	v_mfma_f32_16x16x32_f16 v[42:45], v[86:89], v[102:105], v[42:45]
	v_mfma_f32_16x16x32_f16 v[54:57], v[78:81], v[110:113], v[54:57]
	v_mfma_f32_16x16x32_f16 v[38:41], v[86:89], v[110:113], v[38:41]
	v_mfma_f32_16x16x32_f16 v[50:53], v[78:81], v[118:121], v[50:53]
	v_mfma_f32_16x16x32_f16 v[26:29], v[86:89], v[118:121], v[26:29]
	s_barrier
	s_add_u32 s18, s18, s2
	s_addc_u32 s19, s19, s3
	s_add_i32 m0, s17, 0x8000
	v_lshl_add_u64 v[122:123], s[18:19], 0, v[68:69]
	ds_read_b128 v[74:77], v73 offset:32768
	ds_read_b128 v[78:81], v73 offset:33792
	ds_read_b128 v[82:85], v73 offset:34816
	ds_read_b128 v[86:89], v73 offset:35840
	global_load_lds_dwordx4 v[122:123], off
	v_lshl_add_u64 v[122:123], s[18:19], 0, v[70:71]
	s_add_i32 m0, s17, 0xa000
	s_nop 0
	global_load_lds_dwordx4 v[122:123], off
	s_waitcnt vmcnt(8)
	s_barrier
	s_waitcnt lgkmcnt(0)
	s_waitcnt lgkmcnt(0)
	v_mfma_f32_16x16x32_f16 v[34:37], v[74:77], v[90:93], v[34:37]
	v_mfma_f32_16x16x32_f16 v[14:17], v[82:85], v[90:93], v[14:17]
	v_mfma_f32_16x16x32_f16 v[30:33], v[74:77], v[98:101], v[30:33]
	v_mfma_f32_16x16x32_f16 v[10:13], v[82:85], v[98:101], v[10:13]
	v_mfma_f32_16x16x32_f16 v[22:25], v[74:77], v[106:109], v[22:25]
	v_mfma_f32_16x16x32_f16 v[6:9], v[82:85], v[106:109], v[6:9]
	v_mfma_f32_16x16x32_f16 v[18:21], v[74:77], v[114:117], v[18:21]
	v_mfma_f32_16x16x32_f16 v[2:5], v[82:85], v[114:117], v[2:5]
	v_mfma_f32_16x16x32_f16 v[34:37], v[78:81], v[94:97], v[34:37]
	v_mfma_f32_16x16x32_f16 v[14:17], v[86:89], v[94:97], v[14:17]
	v_mfma_f32_16x16x32_f16 v[30:33], v[78:81], v[102:105], v[30:33]
	v_mfma_f32_16x16x32_f16 v[10:13], v[86:89], v[102:105], v[10:13]
	v_mfma_f32_16x16x32_f16 v[22:25], v[78:81], v[110:113], v[22:25]
	v_mfma_f32_16x16x32_f16 v[6:9], v[86:89], v[110:113], v[6:9]
	v_mfma_f32_16x16x32_f16 v[18:21], v[78:81], v[118:121], v[18:21]
	v_mfma_f32_16x16x32_f16 v[2:5], v[86:89], v[118:121], v[2:5]
	s_barrier
	s_add_i32 s17, s16, 0xc000
	s_cmp_lg_u32 s17, 0x24000
	s_cselect_b32 s18, s17, 0
	s_add_i32 s15, s15, 1
	s_cmp_eq_u32 s8, s15
	s_mov_b32 s17, s16
	s_mov_b32 s16, s18
	s_cbranch_scc0 .LBB3_4
	v_mov_b32_e32 v69, v5
